# retention scan state image ST XOR-swizzled (chunk^=((e>>2)^(e>>3))&1) for conflict-free ds_read_b128; plus v27 changes
# speedup vs baseline: 1.0057x; 1.0036x over previous
.LBB0_441:
	s_cmp_lt_i32 s92, 5
	s_cselect_b64 s[4:5], -1, 0
	s_cmp_gt_i32 s93, 4
	s_cselect_b64 s[6:7], -1, 0
	s_and_b64 s[4:5], s[4:5], s[6:7]
	s_andn2_b64 vcc, exec, s[4:5]
	s_cbranch_vccnz .LBB0_527
	s_cmpk_gt_i32 s89, 0xff
	s_mov_b32 s6, 11
	s_mov_b32 s4, 12
	s_cbranch_scc1 .LBB0_477
	s_lshr_b32 s3, s90, 7
	s_add_u32 s18, s26, 0x32d00000
	s_addc_u32 s19, s27, 0
	s_add_u32 s35, s26, 0x21d00000
	s_addc_u32 s69, s27, 0
	s_add_u32 s74, s26, 0x3d700000
	s_addc_u32 s75, s27, 0
	s_ashr_i32 s7, s6, 31
	s_lshl_b64 s[6:7], s[6:7], 3
	v_and_b32_e32 v2, 15, v250
	s_add_u32 s6, s0, s6
	v_lshl_or_b32 v1, s88, 4, v2
	s_addc_u32 s7, s1, s7
	s_ashr_i32 s5, s4, 31
	v_add_u32_e32 v3, 0xffffff81, v1
	s_lshl_b64 s[4:5], s[4:5], 3
	v_cvt_f32_i32_e32 v176, v3
	v_ashrrev_i32_e32 v3, 1, v250
	s_add_u32 s4, s0, s4
	v_and_b32_e32 v177, -8, v3
	v_bfe_u32 v3, v250, 2, 2
	s_addc_u32 s5, s1, s5
	s_load_dwordx2 s[20:21], s[6:7], 0x0
	s_load_dwordx2 s[22:23], s[4:5], 0x0
	v_or_b32_e32 v3, v177, v3
	s_movk_i32 s6, 0x90
	v_lshlrev_b32_e32 v4, 3, v250
	s_lshl_b32 s5, s88, 12
	v_mul_lo_u32 v3, v3, s6
	v_and_b32_e32 v4, 24, v4
	v_lshl_add_u32 v142, v250, 4, s5
	v_mov_b32_e32 v143, 0
	v_add3_u32 v178, 0, v3, v4
	v_mul_u32_u24_e32 v4, 0x210, v2
	v_ashrrev_i32_e32 v179, 3, v170
	v_lshlrev_b32_e32 v2, 4, v170
	v_add_u32_e32 v144, s5, v142
	v_mov_b32_e32 v145, v143
	v_mul_lo_u32 v8, v1, s6
	v_and_b32_e32 v9, 0x70, v2
	v_mul_lo_u32 v10, v179, s6
	v_lshl_add_u64 v[2:3], s[26:27], 0, v[142:143]
	s_mov_b64 s[6:7], 0x37100000
	v_lshl_add_u64 v[148:149], v[2:3], 0, s[6:7]
	v_lshl_add_u64 v[2:3], s[26:27], 0, v[144:145]
	s_mov_b64 s[6:7], 0x34f00000
	s_and_b32 s4, s90, 0xffffffc0
	v_cvt_f32_u32_e32 v175, v1
	v_lshl_add_u64 v[150:151], v[2:3], 0, s[6:7]
	v_lshlrev_b32_e32 v2, 3, v170
	s_add_i32 s4, s4, 0
	s_add_i32 s8, 0, 0x11400
	v_and_b32_e32 v2, 56, v2
	v_lshlrev_b32_e32 v5, 1, v177
	v_add_u32_e32 v6, s8, v177
	v_add_u32_e32 v7, s4, v177
	s_movk_i32 s4, 0x2100
	v_lshlrev_b32_e32 v3, 1, v2
	s_mov_b32 s41, 0
	v_sub_u32_e32 v171, 0x80, v1
	v_add_u32_e32 v174, 1, v1
	v_cmp_gt_i32_e64 s[4:5], s4, v170
	v_lshl_or_b32 v146, v179, 10, v9
	v_sub_u32_e32 v180, 0x7f, v179
	v_sub_u32_e32 v181, 63, v179
	v_add_u32_e32 v182, 64, v179
	v_mov_b32_e32 v147, v143
	v_lshl_add_u64 v[152:153], s[18:19], 0, v[144:145]
	v_add3_u32 v183, 0, v10, v9
	v_add3_u32 v184, s8, v10, v3
	v_add3_u32 v185, 0, v5, v4
	v_add_u32_e32 v186, 0xfffffe00, v170
	v_lshl_add_u32 v187, v170, 2, 0
	s_mov_b32 s76, 0x800000
	v_mov_b32_e32 v188, 0x42000000
	s_mov_b32 s77, 0xc2fc0000
	v_mov_b32_e32 v189, 0x42800000
	s_movk_i32 s78, 0x1eff
	s_mov_b32 s79, 0xffff0000
	s_mov_b64 s[42:43], 0x1000
	s_movk_i32 s80, 0x7fff
	v_lshlrev_b32_e32 v142, 1, v2
	s_mov_b32 s81, 0x40000
	v_mov_b32_e32 v190, 0xffff
	v_mov_b32_e32 v191, 0xffff0000
	v_not_b32_e32 v192, 63
	v_add_u32_e32 v193, v6, v8
	v_add_u32_e32 v194, v7, v4
	s_mov_b32 s82, s89
	v_lshrrev_b32_e32 v34, 2, v170
	v_lshrrev_b32_e32 v35, 3, v170
	v_xor_b32_e32 v34, v34, v35
	v_and_b32_e32 v34, 1, v34
	v_bfe_u32 v35, v170, 4, 1
	v_lshlrev_b32_e32 v35, 5, v35
	v_sub_u32_e32 v35, 16, v35
	v_mul_lo_u32 v35, v35, v34
	v_add_u32_e32 v185, v185, v35
	v_bfe_u32 v35, v170, 5, 1
	v_lshlrev_b32_e32 v35, 5, v35
	v_sub_u32_e32 v35, 16, v35
	v_mul_lo_u32 v35, v35, v34
	v_add_u32_e32 v194, v194, v35
	s_branch .LBB0_445

.LBB0_2499:
	s_cmp_lt_i32 s92, 33
	s_cselect_b64 s[4:5], -1, 0
	s_cmp_gt_i32 s93, 32
	s_cselect_b64 s[6:7], -1, 0
	s_and_b64 s[4:5], s[4:5], s[6:7]
	s_andn2_b64 vcc, exec, s[4:5]
	s_cbranch_vccnz .LBB0_2587
	s_mov_b32 s75, s89
	s_cmpk_gt_i32 s89, 0xff
	s_mov_b32 s6, 11
	s_mov_b32 s4, 12
	s_cbranch_scc1 .LBB0_2536
	s_lshr_b32 s3, s90, 7
	s_add_u32 s18, s26, 0x32d00000
	s_addc_u32 s19, s27, 0
	s_add_u32 s81, s26, 0x21d00000
	s_addc_u32 s82, s27, 0
	s_add_u32 s83, s26, 0x3d700000
	s_addc_u32 s84, s27, 0
	s_ashr_i32 s7, s6, 31
	s_lshl_b64 s[6:7], s[6:7], 3
	s_add_u32 s6, s0, s6
	s_addc_u32 s7, s1, s7
	s_ashr_i32 s5, s4, 31
	s_lshl_b64 s[4:5], s[4:5], 3
	s_add_u32 s4, s0, s4
	s_addc_u32 s5, s1, s5
	s_load_dwordx2 s[20:21], s[6:7], 0x0
	s_load_dwordx2 s[22:23], s[4:5], 0x0
	v_readlane_b32 s6, v255, 10
	v_and_b32_e32 v1, 15, v250
	s_lshl_b32 s5, s6, 12
	s_waitcnt vmcnt(0)
	v_lshl_or_b32 v65, s6, 4, v1
	v_add_u32_e32 v2, 0xffffff81, v65
	v_cvt_f32_i32_e32 v202, v2
	v_ashrrev_i32_e32 v2, 1, v250
	v_and_b32_e32 v203, -8, v2
	v_bfe_u32 v2, v250, 2, 2
	v_or_b32_e32 v2, v203, v2
	s_movk_i32 s6, 0x90
	v_lshlrev_b32_e32 v3, 3, v250
	v_mul_lo_u32 v2, v2, s6
	v_and_b32_e32 v3, 24, v3
	v_lshl_add_u32 v172, v250, 4, s5
	v_mov_b32_e32 v173, 0
	v_add3_u32 v204, 0, v2, v3
	v_ashrrev_i32_e32 v205, 3, v170
	v_lshlrev_b32_e32 v2, 4, v170
	v_add_u32_e32 v174, s5, v172
	v_mov_b32_e32 v175, v173
	v_mul_lo_u32 v7, v65, s6
	v_and_b32_e32 v8, 0x70, v2
	v_mul_lo_u32 v9, v205, s6
	v_lshl_add_u64 v[2:3], s[26:27], 0, v[172:173]
	s_mov_b64 s[6:7], 0x37100000
	v_lshl_add_u64 v[178:179], v[2:3], 0, s[6:7]
	v_lshl_add_u64 v[2:3], s[26:27], 0, v[174:175]
	s_mov_b64 s[6:7], 0x34f00000
	s_and_b32 s4, s90, 0xffffffc0
	v_cvt_f32_u32_e32 v201, v65
	v_lshl_add_u64 v[182:183], v[2:3], 0, s[6:7]
	v_lshlrev_b32_e32 v2, 3, v170
	s_add_i32 s4, s4, 0
	s_add_i32 s8, 0, 0x11400
	v_and_b32_e32 v2, 56, v2
	v_lshlrev_b32_e32 v4, 1, v203
	v_add_u32_e32 v5, s8, v203
	v_add_u32_e32 v6, s4, v203
	v_mul_u32_u24_e32 v1, 0x210, v1
	s_movk_i32 s4, 0x2100
	v_lshlrev_b32_e32 v3, 1, v2
	s_mov_b32 s41, 0
	v_sub_u32_e32 v171, 0x80, v65
	v_add_u32_e32 v200, 1, v65
	v_cmp_gt_i32_e64 s[4:5], s4, v170
	v_lshl_or_b32 v176, v205, 10, v8
	v_sub_u32_e32 v206, 0x7f, v205
	v_sub_u32_e32 v207, 63, v205
	v_add_u32_e32 v208, 64, v205
	v_mov_b32_e32 v177, v173
	v_lshl_add_u64 v[180:181], s[18:19], 0, v[174:175]
	v_add3_u32 v209, 0, v9, v8
	v_add3_u32 v210, s8, v9, v3
	v_add3_u32 v211, 0, v4, v1
	v_add_u32_e32 v212, 0xfffffe00, v170
	v_lshl_add_u32 v213, v170, 2, 0
	v_mov_b32_e32 v214, 0x42000000
	s_mov_b32 s85, 0xc2fc0000
	v_mov_b32_e32 v215, 0x42800000
	s_mov_b64 s[42:43], 0x1000
	s_mov_b32 s86, 0xffff0000
	s_movk_i32 s87, 0x7fff
	v_lshlrev_b32_e32 v172, 1, v2
	v_add_u32_e32 v216, v5, v7
	v_not_b32_e32 v217, 63
	v_mov_b32_e32 v218, 0xffff
	v_mov_b32_e32 v219, 0xffff0000
	v_add_u32_e32 v220, v6, v1
	s_mov_b32 s88, s75
	v_lshrrev_b32_e32 v2, 2, v170
	v_lshrrev_b32_e32 v3, 3, v170
	v_xor_b32_e32 v2, v2, v3
	v_and_b32_e32 v2, 1, v2
	v_bfe_u32 v3, v170, 4, 1
	v_lshlrev_b32_e32 v3, 5, v3
	v_sub_u32_e32 v3, 16, v3
	v_mul_lo_u32 v3, v3, v2
	v_add_u32_e32 v211, v211, v3
	v_bfe_u32 v3, v170, 5, 1
	v_lshlrev_b32_e32 v3, 5, v3
	v_sub_u32_e32 v3, 16, v3
	v_mul_lo_u32 v3, v3, v2
	v_add_u32_e32 v220, v220, v3
	s_branch .LBB0_2503
